# v44 + grid barrier: non-leader workgroups poll the cross-XCD generation word directly instead of waiting for their XCD leader's relay
# speedup vs baseline: 1.0015x; 1.0015x over previous
; __device__ __forceinline__ unsigned xb_ld(unsigned* p)              { return __hip_atomic_load(p, __ATOMIC_RELAXED, __HIP_MEMORY_SCOPE_AGENT); }
; __device__ __forceinline__ unsigned xb_add(unsigned* p, unsigned v) { return __hip_atomic_fetch_add(p, v, __ATOMIC_RELAXED, __HIP_MEMORY_SCOPE_AGENT); }
; #define XB_SPIN(cond, bar) do { unsigned _sp = 0; while (cond) { __builtin_amdgcn_s_sleep(1); \
;     if ((++_sp & 255u) == 0u) { if (xb_ld(&(bar)[XB_TMO])) break; if (_sp > XB_SPIN_CAP) { atomicAdd(&(bar)[XB_TMO], 1u); break; } } } } while (0)
; __device__ __forceinline__ void xcd_barrier(const XcdBarrier& b) {
;     ...
;         const unsigned old = xb_add(&bar[XB_XSUB(b.x)], 1u);
;         const unsigned gen = old / nloc;
;         if (old + 1u == (gen + 1u) * nloc) {
;             __builtin_amdgcn_fence(__ATOMIC_RELEASE, "agent");
;             asm volatile("s_waitcnt vmcnt(0)" ::: "memory");
;             const unsigned og = xb_add(&bar[XB_TOP], 1u);
;             const unsigned tg = og / nx;
;             if (og + 1u == (tg + 1u) * nx) xb_add(&bar[XB_TOPGEN], 1u);
;             else XB_SPIN(xb_ld(&bar[XB_TOPGEN]) == tg, bar);
;             __builtin_amdgcn_fence(__ATOMIC_ACQUIRE, "agent");
;             xb_add(&bar[XB_XGEN(b.x)], 1u);
;             asm volatile("s_waitcnt vmcnt(0)" ::: "memory");
;         } else {
;             XB_SPIN(xb_ld(&bar[XB_XGEN(b.x)]) == gen, bar);
.LBB0_153:
	s_lshl_b32 s3, s94, 8
	v_readlane_b32 s4, v255, 5
	v_readlane_b32 s5, v255, 6
	s_add_u32 s4, s4, s3
	s_addc_u32 s5, s5, 0
	v_mov_b32_e32 v2, 0x1000
	v_mov_b32_e32 v4, 1
	v_sub_u32_e32 v5, 0, v3
	global_atomic_add v4, v2, v4, s[4:5] offset:1024 sc0
	v_cvt_f32_u32_e32 v2, v3
	v_rcp_iflag_f32_e32 v2, v2
	s_nop 0
	v_mul_f32_e32 v2, 0x4f7ffffe, v2
	v_cvt_u32_f32_e32 v2, v2
	v_mul_lo_u32 v5, v5, v2
	v_mul_hi_u32 v5, v2, v5
	v_add_u32_e32 v2, v2, v5
	s_waitcnt vmcnt(0)
	v_mul_hi_u32 v2, v4, v2
	v_mul_lo_u32 v5, v2, v3
	v_sub_u32_e32 v5, v4, v5
	v_add_u32_e32 v6, 1, v2
	v_cmp_ge_u32_e32 vcc, v5, v3
	v_add_u32_e32 v4, 1, v4
	s_nop 0
	v_cndmask_b32_e32 v2, v2, v6, vcc
	v_sub_u32_e32 v6, v5, v3
	v_cndmask_b32_e32 v5, v5, v6, vcc
	v_add_u32_e32 v6, 1, v2
	v_cmp_ge_u32_e32 vcc, v5, v3
	s_nop 1
	v_cndmask_b32_e32 v2, v2, v6, vcc
	v_mul_lo_u32 v5, v3, v2
	v_add_u32_e32 v3, v5, v3
	v_cmp_ne_u32_e32 vcc, v4, v3
	s_and_saveexec_b64 s[6:7], vcc
	s_xor_b64 s[16:17], exec, s[6:7]
	s_cbranch_execz .LBB0_167
	s_waitcnt lgkmcnt(0)
	v_mov_b32_e32 v1, 0x7100
	global_load_dword v1, v1, s[82:83] offset:1024 sc1
	s_add_u32 s38, s82, 0x7500
	s_addc_u32 s39, s83, 0
	s_waitcnt vmcnt(0)
	v_cmp_eq_u32_e32 vcc, v1, v2
	s_and_saveexec_b64 s[20:21], vcc
	s_cbranch_execz .LBB0_166
	s_add_u32 s24, s82, 0x4200
	s_addc_u32 s25, s83, 0
	s_mov_b32 s3, 1
	s_mov_b64 s[42:43], 0
	v_mov_b32_e32 v1, 0
	s_branch .LBB0_157

; __device__ __forceinline__ unsigned xb_ld(unsigned* p)              { return __hip_atomic_load(p, __ATOMIC_RELAXED, __HIP_MEMORY_SCOPE_AGENT); }
; __device__ __forceinline__ unsigned xb_add(unsigned* p, unsigned v) { return __hip_atomic_fetch_add(p, v, __ATOMIC_RELAXED, __HIP_MEMORY_SCOPE_AGENT); }
; #define XB_SPIN(cond, bar) do { unsigned _sp = 0; while (cond) { __builtin_amdgcn_s_sleep(1); \
;     if ((++_sp & 255u) == 0u) { if (xb_ld(&(bar)[XB_TMO])) break; if (_sp > XB_SPIN_CAP) { atomicAdd(&(bar)[XB_TMO], 1u); break; } } } } while (0)
; __device__ __forceinline__ void xcd_barrier(const XcdBarrier& b) {
;     ...
;         const unsigned old = xb_add(&bar[XB_XSUB(b.x)], 1u);
;         const unsigned gen = old / nloc;
;         if (old + 1u == (gen + 1u) * nloc) {
;             __builtin_amdgcn_fence(__ATOMIC_RELEASE, "agent");
;             asm volatile("s_waitcnt vmcnt(0)" ::: "memory");
;             const unsigned og = xb_add(&bar[XB_TOP], 1u);
;             const unsigned tg = og / nx;
;             if (og + 1u == (tg + 1u) * nx) xb_add(&bar[XB_TOPGEN], 1u);
;             else XB_SPIN(xb_ld(&bar[XB_TOPGEN]) == tg, bar);
;             __builtin_amdgcn_fence(__ATOMIC_ACQUIRE, "agent");
;             xb_add(&bar[XB_XGEN(b.x)], 1u);
;             asm volatile("s_waitcnt vmcnt(0)" ::: "memory");
;         } else {
;             XB_SPIN(xb_ld(&bar[XB_XGEN(b.x)]) == gen, bar);
.LBB0_211:
	s_lshl_b32 s3, s94, 8
	v_readlane_b32 s6, v255, 5
	v_readlane_b32 s7, v255, 6
	s_add_u32 s12, s6, s3
	s_addc_u32 s13, s7, 0
	v_mov_b32_e32 v2, 0x1000
	v_mov_b32_e32 v4, 1
	global_atomic_add v4, v2, v4, s[12:13] offset:1024 sc0
	v_cvt_f32_u32_e32 v2, v3
	v_sub_u32_e32 v5, 0, v3
	v_rcp_iflag_f32_e32 v2, v2
	s_nop 0
	v_mul_f32_e32 v2, 0x4f7ffffe, v2
	v_cvt_u32_f32_e32 v2, v2
	v_mul_lo_u32 v5, v5, v2
	v_mul_hi_u32 v5, v2, v5
	v_add_u32_e32 v2, v2, v5
	s_waitcnt vmcnt(0)
	v_mul_hi_u32 v2, v4, v2
	v_mul_lo_u32 v5, v2, v3
	v_sub_u32_e32 v5, v4, v5
	v_add_u32_e32 v6, 1, v2
	v_cmp_ge_u32_e32 vcc, v5, v3
	v_add_u32_e32 v4, 1, v4
	s_nop 0
	v_cndmask_b32_e32 v2, v2, v6, vcc
	v_sub_u32_e32 v6, v5, v3
	v_cndmask_b32_e32 v5, v5, v6, vcc
	v_add_u32_e32 v6, 1, v2
	v_cmp_ge_u32_e32 vcc, v5, v3
	s_nop 1
	v_cndmask_b32_e32 v2, v2, v6, vcc
	v_mul_lo_u32 v5, v3, v2
	v_add_u32_e32 v3, v5, v3
	v_cmp_ne_u32_e32 vcc, v4, v3
	s_and_saveexec_b64 s[6:7], vcc
	s_xor_b64 s[16:17], exec, s[6:7]
	s_cbranch_execz .LBB0_225
	s_waitcnt lgkmcnt(0)
	v_mov_b32_e32 v1, 0x7100
	global_load_dword v1, v1, s[82:83] offset:1024 sc1
	s_add_u32 s38, s82, 0x7500
	s_addc_u32 s39, s83, 0
	s_waitcnt vmcnt(0)
	v_cmp_eq_u32_e32 vcc, v1, v2
	s_and_saveexec_b64 s[20:21], vcc
	s_cbranch_execz .LBB0_224
	s_add_u32 s24, s82, 0x4200
	s_addc_u32 s25, s83, 0
	s_mov_b32 s3, 1
	s_mov_b64 s[40:41], 0
	v_mov_b32_e32 v1, 0
	s_branch .LBB0_215

; __device__ __forceinline__ unsigned xb_ld(unsigned* p)              { return __hip_atomic_load(p, __ATOMIC_RELAXED, __HIP_MEMORY_SCOPE_AGENT); }
; __device__ __forceinline__ unsigned xb_add(unsigned* p, unsigned v) { return __hip_atomic_fetch_add(p, v, __ATOMIC_RELAXED, __HIP_MEMORY_SCOPE_AGENT); }
; #define XB_SPIN(cond, bar) do { unsigned _sp = 0; while (cond) { __builtin_amdgcn_s_sleep(1); \
;     if ((++_sp & 255u) == 0u) { if (xb_ld(&(bar)[XB_TMO])) break; if (_sp > XB_SPIN_CAP) { atomicAdd(&(bar)[XB_TMO], 1u); break; } } } } while (0)
; __device__ __forceinline__ void xcd_barrier(const XcdBarrier& b) {
;     ...
;         const unsigned old = xb_add(&bar[XB_XSUB(b.x)], 1u);
;         const unsigned gen = old / nloc;
;         if (old + 1u == (gen + 1u) * nloc) {
;             __builtin_amdgcn_fence(__ATOMIC_RELEASE, "agent");
;             asm volatile("s_waitcnt vmcnt(0)" ::: "memory");
;             const unsigned og = xb_add(&bar[XB_TOP], 1u);
;             const unsigned tg = og / nx;
;             if (og + 1u == (tg + 1u) * nx) xb_add(&bar[XB_TOPGEN], 1u);
;             else XB_SPIN(xb_ld(&bar[XB_TOPGEN]) == tg, bar);
;             __builtin_amdgcn_fence(__ATOMIC_ACQUIRE, "agent");
;             xb_add(&bar[XB_XGEN(b.x)], 1u);
;             asm volatile("s_waitcnt vmcnt(0)" ::: "memory");
;         } else {
;             XB_SPIN(xb_ld(&bar[XB_XGEN(b.x)]) == gen, bar);
.LBB0_509:
	s_lshl_b32 s3, s94, 8
	v_readlane_b32 s6, v255, 5
	v_readlane_b32 s7, v255, 6
	s_add_u32 s16, s6, s3
	s_addc_u32 s17, s7, 0
	v_mov_b32_e32 v2, 0x1000
	v_mov_b32_e32 v4, 1
	global_atomic_add v4, v2, v4, s[16:17] offset:1024 sc0
	v_cvt_f32_u32_e32 v2, v3
	v_sub_u32_e32 v5, 0, v3
	v_rcp_iflag_f32_e32 v2, v2
	s_nop 0
	v_mul_f32_e32 v2, 0x4f7ffffe, v2
	v_cvt_u32_f32_e32 v2, v2
	v_mul_lo_u32 v5, v5, v2
	v_mul_hi_u32 v5, v2, v5
	v_add_u32_e32 v2, v2, v5
	s_waitcnt vmcnt(0)
	v_mul_hi_u32 v2, v4, v2
	v_mul_lo_u32 v5, v2, v3
	v_sub_u32_e32 v5, v4, v5
	v_add_u32_e32 v6, 1, v2
	v_cmp_ge_u32_e32 vcc, v5, v3
	v_add_u32_e32 v4, 1, v4
	s_nop 0
	v_cndmask_b32_e32 v2, v2, v6, vcc
	v_sub_u32_e32 v6, v5, v3
	v_cndmask_b32_e32 v5, v5, v6, vcc
	v_add_u32_e32 v6, 1, v2
	v_cmp_ge_u32_e32 vcc, v5, v3
	s_nop 1
	v_cndmask_b32_e32 v2, v2, v6, vcc
	v_mul_lo_u32 v5, v3, v2
	v_add_u32_e32 v3, v5, v3
	v_cmp_ne_u32_e32 vcc, v4, v3
	s_and_saveexec_b64 s[6:7], vcc
	s_xor_b64 s[20:21], exec, s[6:7]
	s_cbranch_execz .LBB0_523
	s_waitcnt lgkmcnt(0)
	v_mov_b32_e32 v1, 0x7100
	global_load_dword v1, v1, s[82:83] offset:1024 sc1
	s_add_u32 s40, s82, 0x7500
	s_addc_u32 s41, s83, 0
	s_waitcnt vmcnt(0)
	v_cmp_eq_u32_e32 vcc, v1, v2
	s_and_saveexec_b64 s[24:25], vcc
	s_cbranch_execz .LBB0_522
	s_add_u32 s38, s82, 0x4200
	s_addc_u32 s39, s83, 0
	s_mov_b32 s3, 1
	s_mov_b64 s[42:43], 0
	v_mov_b32_e32 v1, 0
	s_branch .LBB0_513

; __device__ __forceinline__ unsigned xb_ld(unsigned* p)              { return __hip_atomic_load(p, __ATOMIC_RELAXED, __HIP_MEMORY_SCOPE_AGENT); }
; __device__ __forceinline__ unsigned xb_add(unsigned* p, unsigned v) { return __hip_atomic_fetch_add(p, v, __ATOMIC_RELAXED, __HIP_MEMORY_SCOPE_AGENT); }
; #define XB_SPIN(cond, bar) do { unsigned _sp = 0; while (cond) { __builtin_amdgcn_s_sleep(1); \
;     if ((++_sp & 255u) == 0u) { if (xb_ld(&(bar)[XB_TMO])) break; if (_sp > XB_SPIN_CAP) { atomicAdd(&(bar)[XB_TMO], 1u); break; } } } } while (0)
; __device__ __forceinline__ void xcd_barrier(const XcdBarrier& b) {
;     ...
;         const unsigned old = xb_add(&bar[XB_XSUB(b.x)], 1u);
;         const unsigned gen = old / nloc;
;         if (old + 1u == (gen + 1u) * nloc) {
;             __builtin_amdgcn_fence(__ATOMIC_RELEASE, "agent");
;             asm volatile("s_waitcnt vmcnt(0)" ::: "memory");
;             const unsigned og = xb_add(&bar[XB_TOP], 1u);
;             const unsigned tg = og / nx;
;             if (og + 1u == (tg + 1u) * nx) xb_add(&bar[XB_TOPGEN], 1u);
;             else XB_SPIN(xb_ld(&bar[XB_TOPGEN]) == tg, bar);
;             __builtin_amdgcn_fence(__ATOMIC_ACQUIRE, "agent");
;             xb_add(&bar[XB_XGEN(b.x)], 1u);
;             asm volatile("s_waitcnt vmcnt(0)" ::: "memory");
;         } else {
;             XB_SPIN(xb_ld(&bar[XB_XGEN(b.x)]) == gen, bar);
.LBB0_723:
	s_lshl_b32 s3, s94, 8
	v_readlane_b32 s6, v255, 5
	v_readlane_b32 s7, v255, 6
	s_add_u32 s12, s6, s3
	s_addc_u32 s13, s7, 0
	v_mov_b32_e32 v2, 0x1000
	v_mov_b32_e32 v4, 1
	global_atomic_add v4, v2, v4, s[12:13] offset:1024 sc0
	v_cvt_f32_u32_e32 v2, v3
	v_sub_u32_e32 v5, 0, v3
	v_rcp_iflag_f32_e32 v2, v2
	s_nop 0
	v_mul_f32_e32 v2, 0x4f7ffffe, v2
	v_cvt_u32_f32_e32 v2, v2
	v_mul_lo_u32 v5, v5, v2
	v_mul_hi_u32 v5, v2, v5
	v_add_u32_e32 v2, v2, v5
	s_waitcnt vmcnt(0)
	v_mul_hi_u32 v2, v4, v2
	v_mul_lo_u32 v5, v2, v3
	v_sub_u32_e32 v5, v4, v5
	v_add_u32_e32 v6, 1, v2
	v_cmp_ge_u32_e32 vcc, v5, v3
	v_add_u32_e32 v4, 1, v4
	s_nop 0
	v_cndmask_b32_e32 v2, v2, v6, vcc
	v_sub_u32_e32 v6, v5, v3
	v_cndmask_b32_e32 v5, v5, v6, vcc
	v_add_u32_e32 v6, 1, v2
	v_cmp_ge_u32_e32 vcc, v5, v3
	s_nop 1
	v_cndmask_b32_e32 v2, v2, v6, vcc
	v_mul_lo_u32 v5, v3, v2
	v_add_u32_e32 v3, v5, v3
	v_cmp_ne_u32_e32 vcc, v4, v3
	s_and_saveexec_b64 s[6:7], vcc
	s_xor_b64 s[16:17], exec, s[6:7]
	s_cbranch_execz .LBB0_737
	s_waitcnt lgkmcnt(0)
	v_mov_b32_e32 v1, 0x7100
	global_load_dword v1, v1, s[82:83] offset:1024 sc1
	s_add_u32 s36, s82, 0x7500
	s_addc_u32 s37, s83, 0
	s_waitcnt vmcnt(0)
	v_cmp_eq_u32_e32 vcc, v1, v2
	s_and_saveexec_b64 s[20:21], vcc
	s_cbranch_execz .LBB0_736
	s_add_u32 s24, s82, 0x4200
	s_addc_u32 s25, s83, 0
	s_mov_b32 s3, 1
	s_mov_b64 s[38:39], 0
	v_mov_b32_e32 v1, 0
	s_branch .LBB0_727

; __device__ __forceinline__ unsigned xb_ld(unsigned* p)              { return __hip_atomic_load(p, __ATOMIC_RELAXED, __HIP_MEMORY_SCOPE_AGENT); }
; __device__ __forceinline__ unsigned xb_add(unsigned* p, unsigned v) { return __hip_atomic_fetch_add(p, v, __ATOMIC_RELAXED, __HIP_MEMORY_SCOPE_AGENT); }
; #define XB_SPIN(cond, bar) do { unsigned _sp = 0; while (cond) { __builtin_amdgcn_s_sleep(1); \
;     if ((++_sp & 255u) == 0u) { if (xb_ld(&(bar)[XB_TMO])) break; if (_sp > XB_SPIN_CAP) { atomicAdd(&(bar)[XB_TMO], 1u); break; } } } } while (0)
; __device__ __forceinline__ void xcd_barrier(const XcdBarrier& b) {
;     ...
;         const unsigned old = xb_add(&bar[XB_XSUB(b.x)], 1u);
;         const unsigned gen = old / nloc;
;         if (old + 1u == (gen + 1u) * nloc) {
;             __builtin_amdgcn_fence(__ATOMIC_RELEASE, "agent");
;             asm volatile("s_waitcnt vmcnt(0)" ::: "memory");
;             const unsigned og = xb_add(&bar[XB_TOP], 1u);
;             const unsigned tg = og / nx;
;             if (og + 1u == (tg + 1u) * nx) xb_add(&bar[XB_TOPGEN], 1u);
;             else XB_SPIN(xb_ld(&bar[XB_TOPGEN]) == tg, bar);
;             __builtin_amdgcn_fence(__ATOMIC_ACQUIRE, "agent");
;             xb_add(&bar[XB_XGEN(b.x)], 1u);
;             asm volatile("s_waitcnt vmcnt(0)" ::: "memory");
;         } else {
;             XB_SPIN(xb_ld(&bar[XB_XGEN(b.x)]) == gen, bar);
.LBB0_952:
	s_lshl_b32 s3, s94, 8
	v_readlane_b32 s6, v255, 5
	v_readlane_b32 s7, v255, 6
	s_add_u32 s8, s6, s3
	s_addc_u32 s9, s7, 0
	v_mov_b32_e32 v2, 0x1000
	v_mov_b32_e32 v4, 1
	global_atomic_add v4, v2, v4, s[8:9] offset:1024 sc0
	v_cvt_f32_u32_e32 v2, v3
	v_sub_u32_e32 v5, 0, v3
	v_rcp_iflag_f32_e32 v2, v2
	s_nop 0
	v_mul_f32_e32 v2, 0x4f7ffffe, v2
	v_cvt_u32_f32_e32 v2, v2
	v_mul_lo_u32 v5, v5, v2
	v_mul_hi_u32 v5, v2, v5
	v_add_u32_e32 v2, v2, v5
	s_waitcnt vmcnt(0)
	v_mul_hi_u32 v2, v4, v2
	v_mul_lo_u32 v5, v2, v3
	v_sub_u32_e32 v5, v4, v5
	v_add_u32_e32 v6, 1, v2
	v_cmp_ge_u32_e32 vcc, v5, v3
	v_add_u32_e32 v4, 1, v4
	s_nop 0
	v_cndmask_b32_e32 v2, v2, v6, vcc
	v_sub_u32_e32 v6, v5, v3
	v_cndmask_b32_e32 v5, v5, v6, vcc
	v_add_u32_e32 v6, 1, v2
	v_cmp_ge_u32_e32 vcc, v5, v3
	s_nop 1
	v_cndmask_b32_e32 v2, v2, v6, vcc
	v_mul_lo_u32 v5, v3, v2
	v_add_u32_e32 v3, v5, v3
	v_cmp_ne_u32_e32 vcc, v4, v3
	s_and_saveexec_b64 s[6:7], vcc
	s_xor_b64 s[10:11], exec, s[6:7]
	s_cbranch_execz .LBB0_966
	s_waitcnt lgkmcnt(0)
	v_mov_b32_e32 v1, 0x7100
	global_load_dword v1, v1, s[82:83] offset:1024 sc1
	s_add_u32 s16, s82, 0x7500
	s_addc_u32 s17, s83, 0
	s_waitcnt vmcnt(0)
	v_cmp_eq_u32_e32 vcc, v1, v2
	s_and_saveexec_b64 s[12:13], vcc
	s_cbranch_execz .LBB0_965
	s_add_u32 s14, s82, 0x4200
	s_addc_u32 s15, s83, 0
	s_mov_b32 s3, 1
	s_mov_b64 s[20:21], 0
	v_mov_b32_e32 v1, 0
	s_branch .LBB0_956

; __device__ __forceinline__ unsigned xb_ld(unsigned* p)              { return __hip_atomic_load(p, __ATOMIC_RELAXED, __HIP_MEMORY_SCOPE_AGENT); }
; __device__ __forceinline__ unsigned xb_add(unsigned* p, unsigned v) { return __hip_atomic_fetch_add(p, v, __ATOMIC_RELAXED, __HIP_MEMORY_SCOPE_AGENT); }
; #define XB_SPIN(cond, bar) do { unsigned _sp = 0; while (cond) { __builtin_amdgcn_s_sleep(1); \
;     if ((++_sp & 255u) == 0u) { if (xb_ld(&(bar)[XB_TMO])) break; if (_sp > XB_SPIN_CAP) { atomicAdd(&(bar)[XB_TMO], 1u); break; } } } } while (0)
; __device__ __forceinline__ void xcd_barrier(const XcdBarrier& b) {
;     ...
;         const unsigned old = xb_add(&bar[XB_XSUB(b.x)], 1u);
;         const unsigned gen = old / nloc;
;         if (old + 1u == (gen + 1u) * nloc) {
;             __builtin_amdgcn_fence(__ATOMIC_RELEASE, "agent");
;             asm volatile("s_waitcnt vmcnt(0)" ::: "memory");
;             const unsigned og = xb_add(&bar[XB_TOP], 1u);
;             const unsigned tg = og / nx;
;             if (og + 1u == (tg + 1u) * nx) xb_add(&bar[XB_TOPGEN], 1u);
;             else XB_SPIN(xb_ld(&bar[XB_TOPGEN]) == tg, bar);
;             __builtin_amdgcn_fence(__ATOMIC_ACQUIRE, "agent");
;             xb_add(&bar[XB_XGEN(b.x)], 1u);
;             asm volatile("s_waitcnt vmcnt(0)" ::: "memory");
;         } else {
;             XB_SPIN(xb_ld(&bar[XB_XGEN(b.x)]) == gen, bar);
.LBB0_1062:
	s_lshl_b32 s3, s94, 8
	v_readlane_b32 s6, v255, 5
	v_readlane_b32 s7, v255, 6
	s_add_u32 s10, s6, s3
	s_addc_u32 s11, s7, 0
	v_mov_b32_e32 v2, 0x1000
	v_mov_b32_e32 v4, 1
	global_atomic_add v4, v2, v4, s[10:11] offset:1024 sc0
	v_cvt_f32_u32_e32 v2, v3
	v_sub_u32_e32 v5, 0, v3
	v_rcp_iflag_f32_e32 v2, v2
	s_nop 0
	v_mul_f32_e32 v2, 0x4f7ffffe, v2
	v_cvt_u32_f32_e32 v2, v2
	v_mul_lo_u32 v5, v5, v2
	v_mul_hi_u32 v5, v2, v5
	v_add_u32_e32 v2, v2, v5
	s_waitcnt vmcnt(0)
	v_mul_hi_u32 v2, v4, v2
	v_mul_lo_u32 v5, v2, v3
	v_sub_u32_e32 v5, v4, v5
	v_add_u32_e32 v6, 1, v2
	v_cmp_ge_u32_e32 vcc, v5, v3
	v_add_u32_e32 v4, 1, v4
	s_nop 0
	v_cndmask_b32_e32 v2, v2, v6, vcc
	v_sub_u32_e32 v6, v5, v3
	v_cndmask_b32_e32 v5, v5, v6, vcc
	v_add_u32_e32 v6, 1, v2
	v_cmp_ge_u32_e32 vcc, v5, v3
	s_nop 1
	v_cndmask_b32_e32 v2, v2, v6, vcc
	v_mul_lo_u32 v5, v3, v2
	v_add_u32_e32 v3, v5, v3
	v_cmp_ne_u32_e32 vcc, v4, v3
	s_and_saveexec_b64 s[6:7], vcc
	s_xor_b64 s[12:13], exec, s[6:7]
	s_cbranch_execz .LBB0_1076
	s_waitcnt lgkmcnt(0)
	v_mov_b32_e32 v1, 0x7100
	global_load_dword v1, v1, s[82:83] offset:1024 sc1
	s_add_u32 s18, s82, 0x7500
	s_addc_u32 s19, s83, 0
	s_waitcnt vmcnt(0)
	v_cmp_eq_u32_e32 vcc, v1, v2
	s_and_saveexec_b64 s[14:15], vcc
	s_cbranch_execz .LBB0_1075
	s_add_u32 s16, s82, 0x4200
	s_addc_u32 s17, s83, 0
	s_mov_b32 s3, 1
	s_mov_b64 s[20:21], 0
	v_mov_b32_e32 v1, 0
	s_branch .LBB0_1066

; __device__ __forceinline__ unsigned xb_ld(unsigned* p)              { return __hip_atomic_load(p, __ATOMIC_RELAXED, __HIP_MEMORY_SCOPE_AGENT); }
; __device__ __forceinline__ unsigned xb_add(unsigned* p, unsigned v) { return __hip_atomic_fetch_add(p, v, __ATOMIC_RELAXED, __HIP_MEMORY_SCOPE_AGENT); }
; #define XB_SPIN(cond, bar) do { unsigned _sp = 0; while (cond) { __builtin_amdgcn_s_sleep(1); \
;     if ((++_sp & 255u) == 0u) { if (xb_ld(&(bar)[XB_TMO])) break; if (_sp > XB_SPIN_CAP) { atomicAdd(&(bar)[XB_TMO], 1u); break; } } } } while (0)
; __device__ __forceinline__ void xcd_barrier(const XcdBarrier& b) {
;     ...
;         const unsigned old = xb_add(&bar[XB_XSUB(b.x)], 1u);
;         const unsigned gen = old / nloc;
;         if (old + 1u == (gen + 1u) * nloc) {
;             __builtin_amdgcn_fence(__ATOMIC_RELEASE, "agent");
;             asm volatile("s_waitcnt vmcnt(0)" ::: "memory");
;             const unsigned og = xb_add(&bar[XB_TOP], 1u);
;             const unsigned tg = og / nx;
;             if (og + 1u == (tg + 1u) * nx) xb_add(&bar[XB_TOPGEN], 1u);
;             else XB_SPIN(xb_ld(&bar[XB_TOPGEN]) == tg, bar);
;             __builtin_amdgcn_fence(__ATOMIC_ACQUIRE, "agent");
;             xb_add(&bar[XB_XGEN(b.x)], 1u);
;             asm volatile("s_waitcnt vmcnt(0)" ::: "memory");
;         } else {
;             XB_SPIN(xb_ld(&bar[XB_XGEN(b.x)]) == gen, bar);
.LBB0_1152:
	s_lshl_b32 s4, s94, 8
	v_readlane_b32 s6, v255, 5
	v_readlane_b32 s7, v255, 6
	s_add_u32 s4, s6, s4
	s_addc_u32 s5, s7, 0
	v_mov_b32_e32 v2, 0x1000
	v_mov_b32_e32 v4, 1
	global_atomic_add v4, v2, v4, s[4:5] offset:1024 sc0
	v_cvt_f32_u32_e32 v2, v3
	v_sub_u32_e32 v5, 0, v3
	v_rcp_iflag_f32_e32 v2, v2
	s_nop 0
	v_mul_f32_e32 v2, 0x4f7ffffe, v2
	v_cvt_u32_f32_e32 v2, v2
	v_mul_lo_u32 v5, v5, v2
	v_mul_hi_u32 v5, v2, v5
	v_add_u32_e32 v2, v2, v5
	s_waitcnt vmcnt(0)
	v_mul_hi_u32 v2, v4, v2
	v_mul_lo_u32 v5, v2, v3
	v_sub_u32_e32 v5, v4, v5
	v_add_u32_e32 v6, 1, v2
	v_cmp_ge_u32_e32 vcc, v5, v3
	v_add_u32_e32 v4, 1, v4
	s_nop 0
	v_cndmask_b32_e32 v2, v2, v6, vcc
	v_sub_u32_e32 v6, v5, v3
	v_cndmask_b32_e32 v5, v5, v6, vcc
	v_add_u32_e32 v6, 1, v2
	v_cmp_ge_u32_e32 vcc, v5, v3
	s_nop 1
	v_cndmask_b32_e32 v2, v2, v6, vcc
	v_mul_lo_u32 v5, v3, v2
	v_add_u32_e32 v3, v5, v3
	v_cmp_ne_u32_e32 vcc, v4, v3
	s_and_saveexec_b64 s[6:7], vcc
	s_xor_b64 s[10:11], exec, s[6:7]
	s_cbranch_execz .LBB0_1166
	s_waitcnt lgkmcnt(0)
	v_mov_b32_e32 v1, 0x7100
	global_load_dword v1, v1, s[82:83] offset:1024 sc1
	s_add_u32 s16, s82, 0x7500
	s_addc_u32 s17, s83, 0
	s_waitcnt vmcnt(0)
	v_cmp_eq_u32_e32 vcc, v1, v2
	s_and_saveexec_b64 s[12:13], vcc
	s_cbranch_execz .LBB0_1165
	s_add_u32 s14, s82, 0x4200
	s_addc_u32 s15, s83, 0
	s_mov_b32 s6, 1
	s_mov_b64 s[18:19], 0
	v_mov_b32_e32 v1, 0
	s_branch .LBB0_1156
